# baseline (speedup 1.0000x reference)
.LBB2_12:
	s_waitcnt lgkmcnt(0)
	s_mov_b32 s16, 0
	s_mov_b32 s22, s6
	s_mov_b32 s23, s7
	s_mov_b32 s17, s78
	s_nop 0
	s_nop 0
	s_nop 0
	s_nop 0
	s_nop 0
	s_nop 0
	s_nop 0
	s_nop 0
	s_nop 0
	s_nop 0
	s_nop 0
	s_nop 0
	s_nop 0
	s_nop 0
